# P8/P11 residual epilogues: counted vmcnt waits per row group instead of one vmcnt(0) for all 16 residual loads
# baseline (speedup 1.0000x reference)
.LBB0_1121:
	s_lshl_b32 s4, s63, 8
	v_mov_b32_e32 v108, v0
	s_add_i32 s4, s4, s58
	v_and_b32_e32 v198, 64, v250
	v_and_or_b32 v216, v108, 15, s4
	s_lshl_b32 s4, s56, 8
	v_bfe_u32 v196, v108, 4, 2
	s_or_b32 s4, s4, s59
	v_lshl_or_b32 v214, v196, 3, s4
	v_ashrrev_i32_e32 v215, 31, v214
	v_ashrrev_i32_e32 v217, 31, v216
	v_lshlrev_b64 v[232:233], 1, v[214:215]
	v_lshl_add_u64 v[118:119], s[14:15], 0, v[232:233]
	v_lshlrev_b64 v[234:235], 11, v[216:217]
	v_lshl_add_u64 v[128:129], v[118:119], 0, v[234:235]
	global_load_dwordx4 v[192:195], v[128:129], off
	global_load_dwordx4 v[188:191], v[128:129], off offset:256
	v_or_b32_e32 v228, 16, v216
	v_ashrrev_i32_e32 v229, 31, v228
	v_or_b32_e32 v224, 32, v216
	v_ashrrev_i32_e32 v225, 31, v224
	v_or_b32_e32 v220, 48, v216
	v_lshlrev_b64 v[230:231], 11, v[228:229]
	v_ashrrev_i32_e32 v221, 31, v220
	v_lshl_add_u64 v[128:129], v[118:119], 0, v[230:231]
	v_lshlrev_b64 v[226:227], 11, v[224:225]
	v_add_u32_e32 v218, 0x80, v216
	v_add_u32_e32 v108, 0x90, v216
	global_load_dwordx4 v[184:187], v[128:129], off
	global_load_dwordx4 v[180:183], v[128:129], off offset:256
	v_lshl_add_u64 v[128:129], v[118:119], 0, v[226:227]
	v_lshlrev_b64 v[222:223], 11, v[220:221]
	v_ashrrev_i32_e32 v219, 31, v218
	v_ashrrev_i32_e32 v109, 31, v108
	global_load_dwordx4 v[176:179], v[128:129], off
	global_load_dwordx4 v[172:175], v[128:129], off offset:256
	v_lshl_add_u64 v[128:129], v[118:119], 0, v[222:223]
	v_add_u32_e32 v110, 0xa0, v216
	global_load_dwordx4 v[168:171], v[128:129], off
	global_load_dwordx4 v[164:167], v[128:129], off offset:256
	v_lshlrev_b64 v[128:129], 11, v[218:219]
	v_lshlrev_b64 v[108:109], 11, v[108:109]
	v_ashrrev_i32_e32 v111, 31, v110
	v_lshl_add_u64 v[128:129], v[118:119], 0, v[128:129]
	v_lshl_add_u64 v[108:109], v[118:119], 0, v[108:109]
	v_add_u32_e32 v116, 0xb0, v216
	global_load_dwordx4 v[160:163], v[128:129], off
	global_load_dwordx4 v[156:159], v[128:129], off offset:256
	global_load_dwordx4 v[152:155], v[108:109], off
	global_load_dwordx4 v[148:151], v[108:109], off offset:256
	v_lshlrev_b64 v[108:109], 11, v[110:111]
	v_ashrrev_i32_e32 v117, 31, v116
	v_lshl_add_u64 v[108:109], v[118:119], 0, v[108:109]
	global_load_dwordx4 v[136:139], v[108:109], off
	global_load_dwordx4 v[128:131], v[108:109], off offset:256
	v_lshlrev_b64 v[108:109], 11, v[116:117]
	v_lshl_add_u64 v[108:109], v[118:119], 0, v[108:109]
	global_load_dwordx4 v[116:119], v[108:109], off
	s_nop 0
	global_load_dwordx4 v[108:111], v[108:109], off offset:256
	v_xor_b32_e32 v197, 16, v250
	v_add_u32_e32 v198, 64, v198
	v_cmp_lt_i32_e32 vcc, v197, v198
	s_lshl_b32 s44, s56, 2
	s_ashr_i32 s45, s44, 31
	v_cndmask_b32_e32 v197, v250, v197, vcc
	v_lshlrev_b32_e32 v237, 2, v197
	v_xor_b32_e32 v197, 32, v250
	v_cmp_lt_i32_e32 vcc, v197, v198
	s_waitcnt vmcnt(15)
	v_lshlrev_b32_e32 v198, 16, v194
	v_cndmask_b32_e32 v197, v250, v197, vcc
	v_lshlrev_b32_e32 v238, 2, v197
	v_cmp_eq_u32_e32 vcc, 0, v196
	v_lshlrev_b32_e32 v196, 16, v192
	v_and_b32_e32 v197, 0xffff0000, v192
	v_lshlrev_b32_e32 v192, 16, v193
	v_and_b32_e32 v193, 0xffff0000, v193
	v_and_b32_e32 v199, 0xffff0000, v194
	v_lshlrev_b32_e32 v194, 16, v195
	v_and_b32_e32 v195, 0xffff0000, v195
	v_pk_add_f32 v[144:145], v[144:145], v[196:197]
	v_pk_add_f32 v[146:147], v[146:147], v[192:193]
	v_pk_add_f32 v[192:193], v[142:143], v[194:195]
	v_pk_add_f32 v[142:143], v[140:141], v[198:199]
	v_cvt_pk_bf16_f32 v140, v144, v145
	v_lshl_add_u64 v[144:145], s[14:15], 0, v[234:235]
	v_cvt_pk_bf16_f32 v141, v146, v147
	v_cvt_pk_bf16_f32 v142, v142, v143
	v_cvt_pk_bf16_f32 v143, v192, v193
	v_lshl_add_u64 v[144:145], v[144:145], 0, v[232:233]
	global_store_dwordx4 v[144:145], v[140:143], off
	v_lshlrev_b32_e32 v146, 16, v140
	v_lshlrev_b32_e32 v147, 16, v141
	v_and_b32_e32 v140, 0xffff0000, v140
	v_and_b32_e32 v141, 0xffff0000, v141
	v_mul_f32_e32 v140, v140, v140
	v_mul_f32_e32 v141, v141, v141
	v_lshlrev_b32_e32 v192, 16, v142
	v_and_b32_e32 v142, 0xffff0000, v142
	v_lshlrev_b32_e32 v193, 16, v143
	v_and_b32_e32 v143, 0xffff0000, v143
	v_fmac_f32_e32 v140, v146, v146
	v_fmac_f32_e32 v141, v147, v147
	v_add_f32_e32 v140, v140, v141
	v_mul_f32_e32 v141, v142, v142
	v_mul_f32_e32 v142, v143, v143
	v_fmac_f32_e32 v141, v192, v192
	v_fmac_f32_e32 v142, v193, v193
	v_add_f32_e32 v141, v141, v142
	v_add_f32_e32 v192, v140, v141
	s_waitcnt vmcnt(15)
	v_lshlrev_b32_e32 v140, 16, v188
	v_and_b32_e32 v141, 0xffff0000, v188
	v_lshlrev_b32_e32 v142, 16, v189
	v_and_b32_e32 v143, 0xffff0000, v189
	v_lshlrev_b32_e32 v146, 16, v190
	v_and_b32_e32 v147, 0xffff0000, v190
	v_lshlrev_b32_e32 v188, 16, v191
	v_and_b32_e32 v189, 0xffff0000, v191
	v_pk_add_f32 v[134:135], v[134:135], v[142:143]
	v_pk_add_f32 v[132:133], v[132:133], v[140:141]
	v_pk_add_f32 v[140:141], v[126:127], v[188:189]
	v_pk_add_f32 v[126:127], v[124:125], v[146:147]
	v_cvt_pk_bf16_f32 v124, v132, v133
	v_cvt_pk_bf16_f32 v125, v134, v135
	v_cvt_pk_bf16_f32 v126, v126, v127
	v_cvt_pk_bf16_f32 v127, v140, v141
	global_store_dwordx4 v[144:145], v[124:127], off offset:256
	v_lshlrev_b32_e32 v132, 16, v124
	v_lshlrev_b32_e32 v133, 16, v125
	v_and_b32_e32 v124, 0xffff0000, v124
	v_and_b32_e32 v125, 0xffff0000, v125
	v_mul_f32_e32 v124, v124, v124
	v_mul_f32_e32 v125, v125, v125
	v_lshlrev_b32_e32 v134, 16, v126
	v_and_b32_e32 v126, 0xffff0000, v126
	v_lshlrev_b32_e32 v135, 16, v127
	v_and_b32_e32 v127, 0xffff0000, v127
	v_fmac_f32_e32 v124, v132, v132
	v_fmac_f32_e32 v125, v133, v133
	v_add_f32_e32 v124, v124, v125
	v_mul_f32_e32 v125, v126, v126
	v_mul_f32_e32 v126, v127, v127
	v_fmac_f32_e32 v125, v134, v134
	v_fmac_f32_e32 v126, v135, v135
	v_add_f32_e32 v125, v125, v126
	v_add_f32_e32 v124, v124, v125
	v_add_f32_e32 v124, v192, v124
	ds_bpermute_b32 v125, v237, v124
	s_waitcnt lgkmcnt(0)
	v_add_f32_e32 v124, v124, v125
	ds_bpermute_b32 v125, v238, v124
	s_and_saveexec_b64 s[4:5], vcc
	s_cbranch_execz .LBB0_1123
	v_lshlrev_b64 v[126:127], 6, v[216:217]
	v_lshl_add_u64 v[126:127], s[18:19], 0, v[126:127]
	v_lshl_add_u64 v[126:127], s[44:45], 2, v[126:127]
	s_lshl_b32 s56, s53, 2
	v_lshl_add_u64 v[126:127], v[126:127], 0, s[56:57]
	s_waitcnt lgkmcnt(0)
	v_add_f32_e32 v124, v124, v125
	global_store_dword v[126:127], v124, off
.LBB0_1123:
	s_or_b64 exec, exec, s[4:5]
	s_waitcnt vmcnt(15)
	v_lshlrev_b32_e32 v124, 16, v184
	s_waitcnt lgkmcnt(0)
	v_and_b32_e32 v125, 0xffff0000, v184
	v_lshlrev_b32_e32 v126, 16, v185
	v_and_b32_e32 v127, 0xffff0000, v185
	v_lshlrev_b32_e32 v132, 16, v186
	v_and_b32_e32 v133, 0xffff0000, v186
	v_lshlrev_b32_e32 v134, 16, v187
	v_and_b32_e32 v135, 0xffff0000, v187
	v_pk_add_f32 v[120:121], v[120:121], v[124:125]
	v_pk_add_f32 v[122:123], v[122:123], v[126:127]
	v_pk_add_f32 v[124:125], v[114:115], v[134:135]
	v_pk_add_f32 v[114:115], v[112:113], v[132:133]
	v_cvt_pk_bf16_f32 v112, v120, v121
	v_cvt_pk_bf16_f32 v113, v122, v123
	v_and_b32_e32 v121, 0xffff0000, v112
	v_lshlrev_b32_e32 v120, 16, v112
	v_and_b32_e32 v123, 0xffff0000, v113
	v_mul_f32_e32 v121, v121, v121
	v_cvt_pk_bf16_f32 v114, v114, v115
	v_cvt_pk_bf16_f32 v115, v124, v125
	v_lshlrev_b32_e32 v122, 16, v113
	v_fmac_f32_e32 v121, v120, v120
	v_mul_f32_e32 v120, v123, v123
	v_and_b32_e32 v125, 0xffff0000, v114
	v_and_b32_e32 v127, 0xffff0000, v115
	v_fmac_f32_e32 v120, v122, v122
	v_lshlrev_b32_e32 v124, 16, v114
	v_lshlrev_b32_e32 v126, 16, v115
	v_add_f32_e32 v120, v121, v120
	v_mul_f32_e32 v121, v125, v125
	v_mul_f32_e32 v122, v127, v127
	v_fmac_f32_e32 v121, v124, v124
	v_fmac_f32_e32 v122, v126, v126
	v_add_f32_e32 v121, v121, v122
	v_add_f32_e32 v132, v120, v121
	s_waitcnt vmcnt(14)
	v_lshlrev_b32_e32 v120, 16, v180
	v_and_b32_e32 v121, 0xffff0000, v180
	v_lshlrev_b32_e32 v122, 16, v181
	v_and_b32_e32 v123, 0xffff0000, v181
	v_lshlrev_b32_e32 v124, 16, v182
	v_and_b32_e32 v125, 0xffff0000, v182
	v_lshlrev_b32_e32 v126, 16, v183
	v_and_b32_e32 v127, 0xffff0000, v183
	v_pk_add_f32 v[104:105], v[104:105], v[120:121]
	v_pk_add_f32 v[106:107], v[106:107], v[122:123]
	v_pk_add_f32 v[120:121], v[102:103], v[126:127]
	v_pk_add_f32 v[100:101], v[100:101], v[124:125]
	v_cvt_pk_bf16_f32 v102, v104, v105
	v_cvt_pk_bf16_f32 v103, v106, v107
	v_cvt_pk_bf16_f32 v104, v100, v101
	v_and_b32_e32 v101, 0xffff0000, v102
	v_lshlrev_b32_e32 v100, 16, v102
	v_and_b32_e32 v107, 0xffff0000, v103
	v_mul_f32_e32 v101, v101, v101
	v_cvt_pk_bf16_f32 v105, v120, v121
	v_lshlrev_b32_e32 v106, 16, v103
	v_fmac_f32_e32 v101, v100, v100
	v_mul_f32_e32 v100, v107, v107
	v_and_b32_e32 v121, 0xffff0000, v104
	v_and_b32_e32 v123, 0xffff0000, v105
	v_fmac_f32_e32 v100, v106, v106
	v_lshlrev_b32_e32 v120, 16, v104
	v_lshlrev_b32_e32 v122, 16, v105
	v_add_f32_e32 v100, v101, v100
	v_mul_f32_e32 v101, v121, v121
	v_mul_f32_e32 v106, v123, v123
	v_fmac_f32_e32 v101, v120, v120
	v_fmac_f32_e32 v106, v122, v122
	v_add_f32_e32 v101, v101, v106
	v_add_f32_e32 v100, v100, v101
	v_add_f32_e32 v100, v132, v100
	ds_bpermute_b32 v101, v237, v100
	v_lshl_add_u64 v[106:107], s[14:15], 0, v[230:231]
	v_lshl_add_u64 v[106:107], v[214:215], 1, v[106:107]
	global_store_dwordx4 v[106:107], v[112:115], off
	global_store_dwordx4 v[106:107], v[102:105], off offset:256
	s_waitcnt lgkmcnt(0)
	v_add_f32_e32 v100, v100, v101
	ds_bpermute_b32 v101, v238, v100
	s_and_saveexec_b64 s[4:5], vcc
	s_cbranch_execz .LBB0_1125
	v_lshlrev_b64 v[102:103], 6, v[228:229]
	v_lshl_add_u64 v[102:103], s[18:19], 0, v[102:103]
	v_lshl_add_u64 v[102:103], s[44:45], 2, v[102:103]
	s_lshl_b32 s56, s53, 2
	v_lshl_add_u64 v[102:103], v[102:103], 0, s[56:57]
	s_waitcnt lgkmcnt(0)
	v_add_f32_e32 v100, v100, v101
	global_store_dword v[102:103], v100, off
.LBB0_1125:
	s_or_b64 exec, exec, s[4:5]
	s_waitcnt vmcnt(15)
	v_lshlrev_b32_e32 v100, 16, v176
	s_waitcnt lgkmcnt(0)
	v_and_b32_e32 v101, 0xffff0000, v176
	v_lshlrev_b32_e32 v102, 16, v177
	v_and_b32_e32 v103, 0xffff0000, v177
	v_lshlrev_b32_e32 v104, 16, v178
	v_and_b32_e32 v105, 0xffff0000, v178
	v_lshlrev_b32_e32 v106, 16, v179
	v_and_b32_e32 v107, 0xffff0000, v179
	v_pk_add_f32 v[96:97], v[96:97], v[100:101]
	v_pk_add_f32 v[98:99], v[98:99], v[102:103]
	v_pk_add_f32 v[100:101], v[94:95], v[106:107]
	v_pk_add_f32 v[94:95], v[92:93], v[104:105]
	v_cvt_pk_bf16_f32 v92, v96, v97
	v_cvt_pk_bf16_f32 v93, v98, v99
	v_and_b32_e32 v97, 0xffff0000, v92
	v_lshlrev_b32_e32 v96, 16, v92
	v_and_b32_e32 v99, 0xffff0000, v93
	v_mul_f32_e32 v97, v97, v97
	v_cvt_pk_bf16_f32 v94, v94, v95
	v_cvt_pk_bf16_f32 v95, v100, v101
	v_lshlrev_b32_e32 v98, 16, v93
	v_fmac_f32_e32 v97, v96, v96
	v_mul_f32_e32 v96, v99, v99
	v_and_b32_e32 v101, 0xffff0000, v94
	v_and_b32_e32 v103, 0xffff0000, v95
	v_fmac_f32_e32 v96, v98, v98
	v_lshlrev_b32_e32 v100, 16, v94
	v_lshlrev_b32_e32 v102, 16, v95
	v_add_f32_e32 v96, v97, v96
	v_mul_f32_e32 v97, v101, v101
	v_mul_f32_e32 v98, v103, v103
	v_fmac_f32_e32 v97, v100, v100
	v_fmac_f32_e32 v98, v102, v102
	v_add_f32_e32 v97, v97, v98
	v_add_f32_e32 v104, v96, v97
	s_waitcnt vmcnt(14)
	v_lshlrev_b32_e32 v96, 16, v172
	v_and_b32_e32 v97, 0xffff0000, v172
	v_lshlrev_b32_e32 v98, 16, v173
	v_and_b32_e32 v99, 0xffff0000, v173
	v_lshlrev_b32_e32 v100, 16, v174
	v_and_b32_e32 v101, 0xffff0000, v174
	v_lshlrev_b32_e32 v102, 16, v175
	v_and_b32_e32 v103, 0xffff0000, v175
	v_pk_add_f32 v[88:89], v[88:89], v[96:97]
	v_pk_add_f32 v[90:91], v[90:91], v[98:99]
	v_pk_add_f32 v[96:97], v[86:87], v[102:103]
	v_pk_add_f32 v[84:85], v[84:85], v[100:101]
	v_cvt_pk_bf16_f32 v86, v88, v89
	v_cvt_pk_bf16_f32 v87, v90, v91
	v_cvt_pk_bf16_f32 v88, v84, v85
	v_and_b32_e32 v85, 0xffff0000, v86
	v_lshlrev_b32_e32 v84, 16, v86
	v_and_b32_e32 v91, 0xffff0000, v87
	v_mul_f32_e32 v85, v85, v85
	v_cvt_pk_bf16_f32 v89, v96, v97
	v_lshlrev_b32_e32 v90, 16, v87
	v_fmac_f32_e32 v85, v84, v84
	v_mul_f32_e32 v84, v91, v91
	v_and_b32_e32 v97, 0xffff0000, v88
	v_and_b32_e32 v99, 0xffff0000, v89
	v_fmac_f32_e32 v84, v90, v90
	v_lshlrev_b32_e32 v96, 16, v88
	v_lshlrev_b32_e32 v98, 16, v89
	v_add_f32_e32 v84, v85, v84
	v_mul_f32_e32 v85, v97, v97
	v_mul_f32_e32 v90, v99, v99
	v_fmac_f32_e32 v85, v96, v96
	v_fmac_f32_e32 v90, v98, v98
	v_add_f32_e32 v85, v85, v90
	v_add_f32_e32 v84, v84, v85
	v_add_f32_e32 v84, v104, v84
	ds_bpermute_b32 v85, v237, v84
	v_lshl_add_u64 v[90:91], s[14:15], 0, v[226:227]
	v_lshl_add_u64 v[90:91], v[214:215], 1, v[90:91]
	global_store_dwordx4 v[90:91], v[92:95], off
	global_store_dwordx4 v[90:91], v[86:89], off offset:256
	s_waitcnt lgkmcnt(0)
	v_add_f32_e32 v84, v84, v85
	ds_bpermute_b32 v85, v238, v84
	s_and_saveexec_b64 s[4:5], vcc
	s_mov_b32 s76, 0xe000
	s_movk_i32 s75, 0x3400
	v_readlane_b32 s74, v255, 38
	s_cbranch_execz .LBB0_1127
	v_lshlrev_b64 v[86:87], 6, v[224:225]
	v_lshl_add_u64 v[86:87], s[18:19], 0, v[86:87]
	v_lshl_add_u64 v[86:87], s[44:45], 2, v[86:87]
	s_lshl_b32 s56, s53, 2
	v_lshl_add_u64 v[86:87], v[86:87], 0, s[56:57]
	s_waitcnt lgkmcnt(0)
	v_add_f32_e32 v84, v84, v85
	global_store_dword v[86:87], v84, off
.LBB0_1127:
	s_or_b64 exec, exec, s[4:5]
	s_waitcnt vmcnt(15)
	v_lshlrev_b32_e32 v84, 16, v168
	s_waitcnt lgkmcnt(0)
	v_and_b32_e32 v85, 0xffff0000, v168
	v_lshlrev_b32_e32 v86, 16, v169
	v_and_b32_e32 v87, 0xffff0000, v169
	v_lshlrev_b32_e32 v88, 16, v170
	v_and_b32_e32 v89, 0xffff0000, v170
	v_lshlrev_b32_e32 v90, 16, v171
	v_and_b32_e32 v91, 0xffff0000, v171
	v_pk_add_f32 v[80:81], v[80:81], v[84:85]
	v_pk_add_f32 v[82:83], v[82:83], v[86:87]
	v_pk_add_f32 v[84:85], v[78:79], v[90:91]
	v_pk_add_f32 v[78:79], v[76:77], v[88:89]
	v_cvt_pk_bf16_f32 v76, v80, v81
	v_cvt_pk_bf16_f32 v77, v82, v83
	v_and_b32_e32 v81, 0xffff0000, v76
	v_lshlrev_b32_e32 v80, 16, v76
	v_and_b32_e32 v83, 0xffff0000, v77
	v_mul_f32_e32 v81, v81, v81
	v_cvt_pk_bf16_f32 v78, v78, v79
	v_cvt_pk_bf16_f32 v79, v84, v85
	v_lshlrev_b32_e32 v82, 16, v77
	v_fmac_f32_e32 v81, v80, v80
	v_mul_f32_e32 v80, v83, v83
	v_and_b32_e32 v85, 0xffff0000, v78
	v_and_b32_e32 v87, 0xffff0000, v79
	v_fmac_f32_e32 v80, v82, v82
	v_lshlrev_b32_e32 v84, 16, v78
	v_lshlrev_b32_e32 v86, 16, v79
	v_add_f32_e32 v80, v81, v80
	v_mul_f32_e32 v81, v85, v85
	v_mul_f32_e32 v82, v87, v87
	v_fmac_f32_e32 v81, v84, v84
	v_fmac_f32_e32 v82, v86, v86
	v_add_f32_e32 v81, v81, v82
	v_add_f32_e32 v88, v80, v81
	s_waitcnt vmcnt(14)
	v_lshlrev_b32_e32 v80, 16, v164
	v_and_b32_e32 v81, 0xffff0000, v164
	v_lshlrev_b32_e32 v82, 16, v165
	v_and_b32_e32 v83, 0xffff0000, v165
	v_lshlrev_b32_e32 v84, 16, v166
	v_and_b32_e32 v85, 0xffff0000, v166
	v_lshlrev_b32_e32 v86, 16, v167
	v_and_b32_e32 v87, 0xffff0000, v167
	v_pk_add_f32 v[72:73], v[72:73], v[80:81]
	v_pk_add_f32 v[74:75], v[74:75], v[82:83]
	v_pk_add_f32 v[80:81], v[70:71], v[86:87]
	v_pk_add_f32 v[68:69], v[68:69], v[84:85]
	v_cvt_pk_bf16_f32 v70, v72, v73
	v_cvt_pk_bf16_f32 v71, v74, v75
	v_cvt_pk_bf16_f32 v72, v68, v69
	v_and_b32_e32 v69, 0xffff0000, v70
	v_lshlrev_b32_e32 v68, 16, v70
	v_and_b32_e32 v75, 0xffff0000, v71
	v_mul_f32_e32 v69, v69, v69
	v_cvt_pk_bf16_f32 v73, v80, v81
	v_lshlrev_b32_e32 v74, 16, v71
	v_fmac_f32_e32 v69, v68, v68
	v_mul_f32_e32 v68, v75, v75
	v_and_b32_e32 v81, 0xffff0000, v72
	v_and_b32_e32 v83, 0xffff0000, v73
	v_fmac_f32_e32 v68, v74, v74
	v_lshlrev_b32_e32 v80, 16, v72
	v_lshlrev_b32_e32 v82, 16, v73
	v_add_f32_e32 v68, v69, v68
	v_mul_f32_e32 v69, v81, v81
	v_mul_f32_e32 v74, v83, v83
	v_fmac_f32_e32 v69, v80, v80
	v_fmac_f32_e32 v74, v82, v82
	v_add_f32_e32 v69, v69, v74
	v_add_f32_e32 v68, v68, v69
	v_add_f32_e32 v68, v88, v68
	ds_bpermute_b32 v69, v237, v68
	v_lshl_add_u64 v[74:75], s[14:15], 0, v[222:223]
	v_lshl_add_u64 v[74:75], v[214:215], 1, v[74:75]
	global_store_dwordx4 v[74:75], v[76:79], off
	global_store_dwordx4 v[74:75], v[70:73], off offset:256
	s_waitcnt lgkmcnt(0)
	v_add_f32_e32 v68, v68, v69
	ds_bpermute_b32 v69, v238, v68
	s_and_saveexec_b64 s[4:5], vcc
	s_cbranch_execz .LBB0_1129
	v_lshlrev_b64 v[70:71], 6, v[220:221]
	v_lshl_add_u64 v[70:71], s[18:19], 0, v[70:71]
	v_lshl_add_u64 v[70:71], s[44:45], 2, v[70:71]
	s_lshl_b32 s56, s53, 2
	v_lshl_add_u64 v[70:71], v[70:71], 0, s[56:57]
	s_waitcnt lgkmcnt(0)
	v_add_f32_e32 v68, v68, v69
	global_store_dword v[70:71], v68, off
.LBB0_1129:
	s_or_b64 exec, exec, s[4:5]
	s_waitcnt vmcnt(15)
	v_lshlrev_b32_e32 v68, 16, v160
	s_waitcnt lgkmcnt(0)
	v_and_b32_e32 v69, 0xffff0000, v160
	v_lshlrev_b32_e32 v70, 16, v161
	v_and_b32_e32 v71, 0xffff0000, v161
	v_lshlrev_b32_e32 v72, 16, v162
	v_and_b32_e32 v73, 0xffff0000, v162
	v_lshlrev_b32_e32 v74, 16, v163
	v_and_b32_e32 v75, 0xffff0000, v163
	v_pk_add_f32 v[64:65], v[64:65], v[68:69]
	v_pk_add_f32 v[66:67], v[66:67], v[70:71]
	v_pk_add_f32 v[68:69], v[62:63], v[74:75]
	v_pk_add_f32 v[62:63], v[60:61], v[72:73]
	v_cvt_pk_bf16_f32 v60, v64, v65
	v_cvt_pk_bf16_f32 v61, v66, v67
	v_and_b32_e32 v65, 0xffff0000, v60
	v_lshlrev_b32_e32 v64, 16, v60
	v_and_b32_e32 v67, 0xffff0000, v61
	v_mul_f32_e32 v65, v65, v65
	v_cvt_pk_bf16_f32 v62, v62, v63
	v_cvt_pk_bf16_f32 v63, v68, v69
	v_lshlrev_b32_e32 v66, 16, v61
	v_fmac_f32_e32 v65, v64, v64
	v_mul_f32_e32 v64, v67, v67
	v_and_b32_e32 v69, 0xffff0000, v62
	v_and_b32_e32 v71, 0xffff0000, v63
	v_fmac_f32_e32 v64, v66, v66
	v_lshlrev_b32_e32 v68, 16, v62
	v_lshlrev_b32_e32 v70, 16, v63
	v_add_f32_e32 v64, v65, v64
	v_mul_f32_e32 v65, v69, v69
	v_mul_f32_e32 v66, v71, v71
	v_fmac_f32_e32 v65, v68, v68
	v_fmac_f32_e32 v66, v70, v70
	v_add_f32_e32 v65, v65, v66
	v_add_f32_e32 v72, v64, v65
	s_waitcnt vmcnt(14)
	v_lshlrev_b32_e32 v64, 16, v156
	v_and_b32_e32 v65, 0xffff0000, v156
	v_lshlrev_b32_e32 v66, 16, v157
	v_and_b32_e32 v67, 0xffff0000, v157
	v_lshlrev_b32_e32 v68, 16, v158
	v_and_b32_e32 v69, 0xffff0000, v158
	v_lshlrev_b32_e32 v70, 16, v159
	v_and_b32_e32 v71, 0xffff0000, v159
	v_pk_add_f32 v[56:57], v[56:57], v[64:65]
	v_pk_add_f32 v[58:59], v[58:59], v[66:67]
	v_pk_add_f32 v[64:65], v[54:55], v[70:71]
	v_pk_add_f32 v[52:53], v[52:53], v[68:69]
	v_cvt_pk_bf16_f32 v54, v56, v57
	v_cvt_pk_bf16_f32 v55, v58, v59
	v_cvt_pk_bf16_f32 v56, v52, v53
	v_and_b32_e32 v53, 0xffff0000, v54
	v_lshlrev_b32_e32 v52, 16, v54
	v_and_b32_e32 v59, 0xffff0000, v55
	v_mul_f32_e32 v53, v53, v53
	v_cvt_pk_bf16_f32 v57, v64, v65
	v_lshlrev_b32_e32 v58, 16, v55
	v_fmac_f32_e32 v53, v52, v52
	v_mul_f32_e32 v52, v59, v59
	v_and_b32_e32 v65, 0xffff0000, v56
	v_and_b32_e32 v67, 0xffff0000, v57
	v_fmac_f32_e32 v52, v58, v58
	v_lshlrev_b32_e32 v64, 16, v56
	v_lshlrev_b32_e32 v66, 16, v57
	v_add_f32_e32 v52, v53, v52
	v_mul_f32_e32 v53, v65, v65
	v_mul_f32_e32 v58, v67, v67
	v_fmac_f32_e32 v53, v64, v64
	v_fmac_f32_e32 v58, v66, v66
	v_add_f32_e32 v53, v53, v58
	v_add_f32_e32 v52, v52, v53
	v_add_f32_e32 v52, v72, v52
	ds_bpermute_b32 v53, v237, v52
	v_lshlrev_b64 v[58:59], 10, v[218:219]
	v_lshl_add_u64 v[58:59], v[58:59], 1, s[14:15]
	v_lshl_add_u64 v[58:59], v[214:215], 1, v[58:59]
	global_store_dwordx4 v[58:59], v[60:63], off
	global_store_dwordx4 v[58:59], v[54:57], off offset:256
	s_waitcnt lgkmcnt(0)
	v_add_f32_e32 v52, v52, v53
	ds_bpermute_b32 v53, v238, v52
	s_and_saveexec_b64 s[4:5], vcc
	s_cbranch_execz .LBB0_1131
	v_lshlrev_b64 v[54:55], 6, v[218:219]
	v_lshl_add_u64 v[54:55], s[18:19], 0, v[54:55]
	v_lshl_add_u64 v[54:55], s[44:45], 2, v[54:55]
	s_lshl_b32 s56, s53, 2
	v_lshl_add_u64 v[54:55], v[54:55], 0, s[56:57]
	s_waitcnt lgkmcnt(0)
	v_add_f32_e32 v52, v52, v53
	global_store_dword v[54:55], v52, off
.LBB0_1131:
	s_or_b64 exec, exec, s[4:5]
	s_waitcnt vmcnt(15)
	v_lshlrev_b32_e32 v52, 16, v152
	s_waitcnt lgkmcnt(0)
	v_and_b32_e32 v53, 0xffff0000, v152
	v_lshlrev_b32_e32 v54, 16, v153
	v_and_b32_e32 v55, 0xffff0000, v153
	v_lshlrev_b32_e32 v56, 16, v154
	v_and_b32_e32 v57, 0xffff0000, v154
	v_lshlrev_b32_e32 v58, 16, v155
	v_and_b32_e32 v59, 0xffff0000, v155
	v_pk_add_f32 v[48:49], v[48:49], v[52:53]
	v_pk_add_f32 v[50:51], v[50:51], v[54:55]
	v_pk_add_f32 v[52:53], v[46:47], v[58:59]
	v_pk_add_f32 v[46:47], v[44:45], v[56:57]
	v_cvt_pk_bf16_f32 v44, v48, v49
	v_cvt_pk_bf16_f32 v45, v50, v51
	v_and_b32_e32 v49, 0xffff0000, v44
	v_lshlrev_b32_e32 v48, 16, v44
	v_and_b32_e32 v51, 0xffff0000, v45
	v_mul_f32_e32 v49, v49, v49
	v_cvt_pk_bf16_f32 v46, v46, v47
	v_cvt_pk_bf16_f32 v47, v52, v53
	v_lshlrev_b32_e32 v50, 16, v45
	v_fmac_f32_e32 v49, v48, v48
	v_mul_f32_e32 v48, v51, v51
	v_and_b32_e32 v53, 0xffff0000, v46
	v_and_b32_e32 v55, 0xffff0000, v47
	v_fmac_f32_e32 v48, v50, v50
	v_lshlrev_b32_e32 v52, 16, v46
	v_lshlrev_b32_e32 v54, 16, v47
	v_add_f32_e32 v48, v49, v48
	v_mul_f32_e32 v49, v53, v53
	v_mul_f32_e32 v50, v55, v55
	v_fmac_f32_e32 v49, v52, v52
	v_fmac_f32_e32 v50, v54, v54
	v_add_f32_e32 v49, v49, v50
	v_add_f32_e32 v56, v48, v49
	s_waitcnt vmcnt(14)
	v_lshlrev_b32_e32 v48, 16, v148
	v_and_b32_e32 v49, 0xffff0000, v148
	v_lshlrev_b32_e32 v50, 16, v149
	v_and_b32_e32 v51, 0xffff0000, v149
	v_lshlrev_b32_e32 v52, 16, v150
	v_and_b32_e32 v53, 0xffff0000, v150
	v_pk_add_f32 v[40:41], v[40:41], v[48:49]
	v_lshlrev_b32_e32 v54, 16, v151
	v_and_b32_e32 v55, 0xffff0000, v151
	v_pk_add_f32 v[42:43], v[42:43], v[50:51]
	v_pk_add_f32 v[36:37], v[36:37], v[52:53]
	v_cvt_pk_bf16_f32 v40, v40, v41
	v_pk_add_f32 v[38:39], v[38:39], v[54:55]
	v_cvt_pk_bf16_f32 v41, v42, v43
	v_cvt_pk_bf16_f32 v42, v36, v37
	v_and_b32_e32 v37, 0xffff0000, v40
	v_cvt_pk_bf16_f32 v43, v38, v39
	v_lshlrev_b32_e32 v36, 16, v40
	v_and_b32_e32 v39, 0xffff0000, v41
	v_mul_f32_e32 v37, v37, v37
	v_lshlrev_b32_e32 v38, 16, v41
	v_fmac_f32_e32 v37, v36, v36
	v_mul_f32_e32 v36, v39, v39
	v_and_b32_e32 v49, 0xffff0000, v42
	v_and_b32_e32 v51, 0xffff0000, v43
	v_fmac_f32_e32 v36, v38, v38
	v_lshlrev_b32_e32 v48, 16, v42
	v_lshlrev_b32_e32 v50, 16, v43
	v_add_f32_e32 v36, v37, v36
	v_mul_f32_e32 v37, v49, v49
	v_mul_f32_e32 v38, v51, v51
	v_fmac_f32_e32 v37, v48, v48
	v_fmac_f32_e32 v38, v50, v50
	v_add_f32_e32 v37, v37, v38
	v_add_f32_e32 v36, v36, v37
	v_add_f32_e32 v38, v56, v36
	ds_bpermute_b32 v39, v237, v38
	v_add_u32_e32 v36, 0x90, v216
	v_ashrrev_i32_e32 v37, 31, v36
	v_lshlrev_b64 v[48:49], 11, v[36:37]
	v_lshl_add_u64 v[48:49], s[14:15], 0, v[48:49]
	s_waitcnt lgkmcnt(0)
	v_add_f32_e32 v38, v38, v39
	ds_bpermute_b32 v39, v238, v38
	v_lshl_add_u64 v[48:49], v[214:215], 1, v[48:49]
	global_store_dwordx4 v[48:49], v[44:47], off
	global_store_dwordx4 v[48:49], v[40:43], off offset:256
	s_and_saveexec_b64 s[4:5], vcc
	s_cbranch_execz .LBB0_1133
	v_lshlrev_b64 v[36:37], 6, v[36:37]
	v_lshl_add_u64 v[36:37], s[18:19], 0, v[36:37]
	v_lshl_add_u64 v[36:37], s[44:45], 2, v[36:37]
	s_lshl_b32 s56, s53, 2
	v_lshl_add_u64 v[36:37], v[36:37], 0, s[56:57]
	s_waitcnt lgkmcnt(0)
	v_add_f32_e32 v38, v38, v39
	global_store_dword v[36:37], v38, off
.LBB0_1133:
	s_or_b64 exec, exec, s[4:5]
	s_waitcnt vmcnt(15)
	v_lshlrev_b32_e32 v36, 16, v136
	v_and_b32_e32 v37, 0xffff0000, v136
	v_lshlrev_b32_e32 v38, 16, v137
	s_waitcnt lgkmcnt(0)
	v_and_b32_e32 v39, 0xffff0000, v137
	v_lshlrev_b32_e32 v40, 16, v138
	v_and_b32_e32 v41, 0xffff0000, v138
	v_lshlrev_b32_e32 v42, 16, v139
	v_and_b32_e32 v43, 0xffff0000, v139
	v_pk_add_f32 v[32:33], v[32:33], v[36:37]
	v_pk_add_f32 v[34:35], v[34:35], v[38:39]
	v_pk_add_f32 v[36:37], v[30:31], v[42:43]
	v_pk_add_f32 v[30:31], v[28:29], v[40:41]
	v_cvt_pk_bf16_f32 v28, v32, v33
	v_cvt_pk_bf16_f32 v29, v34, v35
	v_and_b32_e32 v33, 0xffff0000, v28
	v_lshlrev_b32_e32 v32, 16, v28
	v_and_b32_e32 v35, 0xffff0000, v29
	v_mul_f32_e32 v33, v33, v33
	v_cvt_pk_bf16_f32 v30, v30, v31
	v_cvt_pk_bf16_f32 v31, v36, v37
	v_lshlrev_b32_e32 v34, 16, v29
	v_fmac_f32_e32 v33, v32, v32
	v_mul_f32_e32 v32, v35, v35
	v_and_b32_e32 v37, 0xffff0000, v30
	v_and_b32_e32 v39, 0xffff0000, v31
	v_fmac_f32_e32 v32, v34, v34
	v_lshlrev_b32_e32 v36, 16, v30
	v_lshlrev_b32_e32 v38, 16, v31
	v_add_f32_e32 v32, v33, v32
	v_mul_f32_e32 v33, v37, v37
	v_mul_f32_e32 v34, v39, v39
	v_fmac_f32_e32 v33, v36, v36
	v_fmac_f32_e32 v34, v38, v38
	v_add_f32_e32 v33, v33, v34
	v_add_f32_e32 v40, v32, v33
	s_waitcnt vmcnt(14)
	v_lshlrev_b32_e32 v32, 16, v128
	v_and_b32_e32 v33, 0xffff0000, v128
	v_lshlrev_b32_e32 v34, 16, v129
	v_and_b32_e32 v35, 0xffff0000, v129
	v_lshlrev_b32_e32 v36, 16, v130
	v_and_b32_e32 v37, 0xffff0000, v130
	v_pk_add_f32 v[24:25], v[24:25], v[32:33]
	v_lshlrev_b32_e32 v38, 16, v131
	v_and_b32_e32 v39, 0xffff0000, v131
	v_pk_add_f32 v[26:27], v[26:27], v[34:35]
	v_pk_add_f32 v[20:21], v[20:21], v[36:37]
	v_cvt_pk_bf16_f32 v24, v24, v25
	v_pk_add_f32 v[22:23], v[22:23], v[38:39]
	v_cvt_pk_bf16_f32 v25, v26, v27
	v_cvt_pk_bf16_f32 v26, v20, v21
	v_and_b32_e32 v21, 0xffff0000, v24
	v_cvt_pk_bf16_f32 v27, v22, v23
	v_lshlrev_b32_e32 v20, 16, v24
	v_and_b32_e32 v23, 0xffff0000, v25
	v_mul_f32_e32 v21, v21, v21
	v_lshlrev_b32_e32 v22, 16, v25
	v_fmac_f32_e32 v21, v20, v20
	v_mul_f32_e32 v20, v23, v23
	v_and_b32_e32 v33, 0xffff0000, v26
	v_and_b32_e32 v35, 0xffff0000, v27
	v_fmac_f32_e32 v20, v22, v22
	v_lshlrev_b32_e32 v32, 16, v26
	v_lshlrev_b32_e32 v34, 16, v27
	v_add_f32_e32 v20, v21, v20
	v_mul_f32_e32 v21, v33, v33
	v_mul_f32_e32 v22, v35, v35
	v_fmac_f32_e32 v21, v32, v32
	v_fmac_f32_e32 v22, v34, v34
	v_add_f32_e32 v21, v21, v22
	v_add_f32_e32 v20, v20, v21
	v_add_f32_e32 v22, v40, v20
	ds_bpermute_b32 v23, v237, v22
	v_add_u32_e32 v20, 0xa0, v216
	v_ashrrev_i32_e32 v21, 31, v20
	v_lshlrev_b64 v[32:33], 11, v[20:21]
	v_lshl_add_u64 v[32:33], s[14:15], 0, v[32:33]
	s_waitcnt lgkmcnt(0)
	v_add_f32_e32 v22, v22, v23
	ds_bpermute_b32 v23, v238, v22
	v_lshl_add_u64 v[32:33], v[214:215], 1, v[32:33]
	global_store_dwordx4 v[32:33], v[28:31], off
	global_store_dwordx4 v[32:33], v[24:27], off offset:256
	s_and_saveexec_b64 s[4:5], vcc
	s_cbranch_execz .LBB0_1135
	v_lshlrev_b64 v[20:21], 6, v[20:21]
	v_lshl_add_u64 v[20:21], s[18:19], 0, v[20:21]
	v_lshl_add_u64 v[20:21], s[44:45], 2, v[20:21]
	s_lshl_b32 s56, s53, 2
	v_lshl_add_u64 v[20:21], v[20:21], 0, s[56:57]
	s_waitcnt lgkmcnt(0)
	v_add_f32_e32 v22, v22, v23
	global_store_dword v[20:21], v22, off
.LBB0_1135:
	s_or_b64 exec, exec, s[4:5]
	s_waitcnt vmcnt(15)
	v_lshlrev_b32_e32 v20, 16, v116
	v_and_b32_e32 v21, 0xffff0000, v116
	v_lshlrev_b32_e32 v22, 16, v117
	s_waitcnt lgkmcnt(0)
	v_and_b32_e32 v23, 0xffff0000, v117
	v_lshlrev_b32_e32 v24, 16, v118
	v_and_b32_e32 v25, 0xffff0000, v118
	v_lshlrev_b32_e32 v26, 16, v119
	v_and_b32_e32 v27, 0xffff0000, v119
	v_pk_add_f32 v[16:17], v[16:17], v[20:21]
	v_pk_add_f32 v[18:19], v[18:19], v[22:23]
	v_pk_add_f32 v[20:21], v[14:15], v[26:27]
	v_pk_add_f32 v[14:15], v[12:13], v[24:25]
	v_cvt_pk_bf16_f32 v12, v16, v17
	v_cvt_pk_bf16_f32 v13, v18, v19
	v_and_b32_e32 v17, 0xffff0000, v12
	v_lshlrev_b32_e32 v16, 16, v12
	v_and_b32_e32 v19, 0xffff0000, v13
	v_mul_f32_e32 v17, v17, v17
	v_cvt_pk_bf16_f32 v14, v14, v15
	v_cvt_pk_bf16_f32 v15, v20, v21
	v_lshlrev_b32_e32 v18, 16, v13
	v_fmac_f32_e32 v17, v16, v16
	v_mul_f32_e32 v16, v19, v19
	v_and_b32_e32 v21, 0xffff0000, v14
	v_and_b32_e32 v23, 0xffff0000, v15
	v_fmac_f32_e32 v16, v18, v18
	v_lshlrev_b32_e32 v20, 16, v14
	v_lshlrev_b32_e32 v22, 16, v15
	v_add_f32_e32 v16, v17, v16
	v_mul_f32_e32 v17, v21, v21
	v_mul_f32_e32 v18, v23, v23
	v_fmac_f32_e32 v17, v20, v20
	v_fmac_f32_e32 v18, v22, v22
	v_add_f32_e32 v17, v17, v18
	v_add_f32_e32 v24, v16, v17
	s_waitcnt vmcnt(14)
	v_lshlrev_b32_e32 v16, 16, v108
	v_and_b32_e32 v17, 0xffff0000, v108
	v_lshlrev_b32_e32 v18, 16, v109
	v_and_b32_e32 v19, 0xffff0000, v109
	v_lshlrev_b32_e32 v20, 16, v110
	v_and_b32_e32 v21, 0xffff0000, v110
	v_pk_add_f32 v[8:9], v[8:9], v[16:17]
	v_lshlrev_b32_e32 v22, 16, v111
	v_and_b32_e32 v23, 0xffff0000, v111
	v_pk_add_f32 v[10:11], v[10:11], v[18:19]
	v_pk_add_f32 v[4:5], v[4:5], v[20:21]
	v_cvt_pk_bf16_f32 v8, v8, v9
	v_pk_add_f32 v[6:7], v[6:7], v[22:23]
	v_cvt_pk_bf16_f32 v9, v10, v11
	v_cvt_pk_bf16_f32 v10, v4, v5
	v_and_b32_e32 v5, 0xffff0000, v8
	v_cvt_pk_bf16_f32 v11, v6, v7
	v_lshlrev_b32_e32 v4, 16, v8
	v_and_b32_e32 v7, 0xffff0000, v9
	v_mul_f32_e32 v5, v5, v5
	v_lshlrev_b32_e32 v6, 16, v9
	v_fmac_f32_e32 v5, v4, v4
	v_mul_f32_e32 v4, v7, v7
	v_and_b32_e32 v17, 0xffff0000, v10
	v_and_b32_e32 v19, 0xffff0000, v11
	v_fmac_f32_e32 v4, v6, v6
	v_lshlrev_b32_e32 v16, 16, v10
	v_lshlrev_b32_e32 v18, 16, v11
	v_add_f32_e32 v4, v5, v4
	v_mul_f32_e32 v5, v17, v17
	v_mul_f32_e32 v6, v19, v19
	v_fmac_f32_e32 v5, v16, v16
	v_fmac_f32_e32 v6, v18, v18
	v_add_f32_e32 v5, v5, v6
	v_add_f32_e32 v4, v4, v5
	v_add_f32_e32 v6, v24, v4
	ds_bpermute_b32 v7, v237, v6
	v_add_u32_e32 v4, 0xb0, v216
	v_ashrrev_i32_e32 v5, 31, v4
	v_lshlrev_b64 v[16:17], 11, v[4:5]
	v_lshl_add_u64 v[16:17], s[14:15], 0, v[16:17]
	s_waitcnt lgkmcnt(0)
	v_add_f32_e32 v6, v6, v7
	ds_bpermute_b32 v7, v238, v6
	v_lshl_add_u64 v[16:17], v[214:215], 1, v[16:17]
	global_store_dwordx4 v[16:17], v[12:15], off
	global_store_dwordx4 v[16:17], v[8:11], off offset:256
	s_and_saveexec_b64 s[4:5], vcc
	s_cbranch_execz .LBB0_1137
	v_lshlrev_b64 v[4:5], 6, v[4:5]
	v_lshl_add_u64 v[4:5], s[18:19], 0, v[4:5]
	v_lshl_add_u64 v[4:5], s[44:45], 2, v[4:5]
	s_lshl_b32 s56, s53, 2
	v_lshl_add_u64 v[4:5], v[4:5], 0, s[56:57]
	s_waitcnt lgkmcnt(0)
	v_add_f32_e32 v6, v6, v7
	global_store_dword v[4:5], v6, off
